# speedup vs baseline: 1.0308x; 1.0308x over previous
_Z11attn_kernelILi0EEvPKDF16_S1_S1_PKfS3_PfPDF16_:
	v_readfirstlane_b32 s3, v0
	s_lshr_b32 s14, s3, 6
	s_lshl_b32 s3, s2, 7
	s_lshr_b32 s12, s2, 4
	s_and_b32 s3, s3, 0x780
	s_lshl_b32 s4, s14, 5
	s_mov_b32 s13, 0
	s_load_dwordx4 s[8:11], s[0:1], 0x0
	s_load_dwordx2 s[18:19], s[0:1], 0x10
	s_add_i32 s3, s4, s3
	s_lshl_b64 s[4:5], s[12:13], 11
	s_add_u32 s16, s4, s3
	s_addc_u32 s17, s5, 0
	s_lshl_b64 s[4:5], s[16:17], 7
	v_and_b32_e32 v164, 31, v0
	s_waitcnt lgkmcnt(0)
	s_add_u32 s4, s8, s4
	v_bfe_u32 v72, v0, 5, 1
	s_addc_u32 s5, s9, s5
	s_lshl_b64 s[22:23], s[12:13], 18
	v_lshlrev_b32_e32 v128, 7, v164
	v_mov_b32_e32 v129, 0
	s_add_u32 s8, s10, s22
	v_lshl_add_u64 v[2:3], s[4:5], 0, v[128:129]
	v_lshlrev_b32_e32 v128, 4, v72
	s_addc_u32 s9, s11, s23
	v_lshl_add_u64 v[10:11], v[2:3], 0, v[128:129]
	v_or_b32_e32 v12, 0x100, v0
	v_lshlrev_b32_e32 v128, 4, v0
	v_lshlrev_b32_e32 v44, 4, v12
	global_load_dwordx4 v[2:5], v128, s[8:9]
	global_load_dwordx4 v[6:9], v44, s[8:9]
	v_lshlrev_b32_e32 v79, 3, v0
	s_movk_i32 s4, 0x48
	v_lshrrev_b32_e32 v73, 3, v0
	v_and_b32_e32 v74, 56, v79
	v_lshrrev_b32_e32 v75, 3, v12
	v_mad_u32_u24 v165, v75, s4, v74
	v_mad_u32_u24 v166, v73, s4, v74
	global_load_dwordx4 v[108:111], v[10:11], off
	global_load_dwordx4 v[104:107], v[10:11], off offset:32
	global_load_dwordx4 v[100:103], v[10:11], off offset:64
	global_load_dwordx4 v[96:99], v[10:11], off offset:96
	v_mov_b32_e32 v86, v44
	s_add_u32 s24, s8, 0x2000
	s_addc_u32 s25, s9, 0
	global_load_dwordx4 v[120:123], v128, s[24:25]
	global_load_dwordx4 v[124:127], v44, s[24:25]
	s_add_u32 s24, s24, 0x2000
	s_addc_u32 s25, s25, 0
	global_load_dwordx4 v[146:149], v128, s[24:25]
	global_load_dwordx4 v[150:153], v44, s[24:25]
	s_add_u32 s24, s24, 0x2000
	s_addc_u32 s25, s25, 0
	global_load_dwordx4 v[154:157], v128, s[24:25]
	global_load_dwordx4 v[158:161], v44, s[24:25]
	s_add_u32 s24, s24, 0x2000
	s_addc_u32 s25, s25, 0
	s_add_u32 s4, s8, 0x2000
	v_lshlrev_b32_e32 v13, 1, v166
	s_addc_u32 s5, s9, 0
	v_lshlrev_b32_e32 v14, 1, v165
	v_lshlrev_b32_e32 v1, 3, v72
	v_mul_u32_u24_e32 v76, 0x48, v164
	v_lshlrev_b32_e32 v80, 3, v12
	v_mov_b32_e32 v45, v129
	s_mov_b32 s15, 1
	v_add_u32_e32 v77, 0x6000, v13
	v_add_u32_e32 v78, 0x6000, v14
	s_waitcnt vmcnt(11)
	ds_write_b128 v13, v[2:5] offset:24576
	s_waitcnt vmcnt(10)
	ds_write_b128 v14, v[6:9] offset:24576
	s_waitcnt lgkmcnt(0)
	s_barrier
	s_load_dwordx4 s[4:7], s[0:1], 0x28
	v_add_lshl_u32 v3, v1, v76, 1
	v_lshl_add_u64 v[68:69], s[8:9], 0, v[44:45]
	v_lshl_add_u64 v[66:67], s[8:9], 0, v[128:129]
	v_add_u32_e32 v167, 0x6000, v3
	v_mov_b32_e32 v87, v3
	v_lshlrev_b32_e32 v88, 1, v166
	v_lshlrev_b32_e32 v89, 1, v165
	s_lshl_b64 s[20:21], s[12:13], 17
	v_mov_b32_e32 v81, 0
	v_mov_b32_e32 v82, 0
	v_mov_b32_e32 v130, 0
	v_mov_b32_e32 v131, 0
	v_mov_b32_e32 v132, 0
	v_mov_b32_e32 v133, 0
	v_mov_b32_e32 v134, 0
	v_mov_b32_e32 v135, 0
	v_mov_b32_e32 v136, 0
	v_mov_b32_e32 v137, 0
	v_mov_b32_e32 v138, 0
	v_mov_b32_e32 v139, 0
	v_mov_b32_e32 v140, 0
	v_mov_b32_e32 v141, 0
	v_mov_b32_e32 v142, 0
	v_mov_b32_e32 v143, 0
	v_mov_b32_e32 v144, 0
	v_mov_b32_e32 v145, 0
	v_mov_b32_e32 v34, 0xff800000
	v_mov_b32_e32 v35, v34
	v_mov_b32_e32 v36, v34
	v_mov_b32_e32 v37, v34
	v_mov_b32_e32 v38, v34
	v_mov_b32_e32 v39, v34
	v_mov_b32_e32 v40, v34
	v_mov_b32_e32 v41, v34
	v_mov_b32_e32 v42, v34
	v_mov_b32_e32 v43, v34
	v_mov_b32_e32 v44, v34
	v_mov_b32_e32 v45, v34
	v_mov_b32_e32 v46, v34
	v_mov_b32_e32 v47, v34
	v_mov_b32_e32 v48, v34
	v_mov_b32_e32 v49, v34
	v_mov_b32_e32 v50, v34
	v_mov_b32_e32 v51, v34
	v_mov_b32_e32 v52, v34
	v_mov_b32_e32 v53, v34
	v_mov_b32_e32 v54, v34
	v_mov_b32_e32 v55, v34
	v_mov_b32_e32 v56, v34
	v_mov_b32_e32 v57, v34
	v_mov_b32_e32 v58, v34
	v_mov_b32_e32 v59, v34
	v_mov_b32_e32 v60, v34
	v_mov_b32_e32 v61, v34
	v_mov_b32_e32 v62, v34
	v_mov_b32_e32 v63, v34
	v_mov_b32_e32 v64, v34
	v_mov_b32_e32 v65, v34
	s_mov_b32 s11, 0xff800000
	s_mov_b32 s15, 0
	s_waitcnt vmcnt(4) lgkmcnt(0)
	ds_write_b128 v77, v[120:123] offset:9216
	ds_write_b128 v78, v[124:127] offset:9216
	s_waitcnt lgkmcnt(0)
	s_barrier
.Lp1_loop:
	s_waitcnt vmcnt(0)
	ds_write_b128 v88, v[146:149]
	ds_write_b128 v89, v[150:153]
	ds_write_b128 v88, v[154:157] offset:9216
	ds_write_b128 v89, v[158:161] offset:9216
	global_load_dwordx4 v[112:115], v128, s[24:25]
	global_load_dwordx4 v[116:119], v86, s[24:25]
	s_add_u32 s24, s24, 0x2000
	s_addc_u32 s25, s25, 0
	global_load_dwordx4 v[120:123], v128, s[24:25]
	global_load_dwordx4 v[124:127], v86, s[24:25]
	s_add_u32 s24, s24, 0x2000
	s_addc_u32 s25, s25, 0
	ds_read_b128 v[168:171], v167
	ds_read_b128 v[172:175], v167 offset:4608
	ds_read_b128 v[176:179], v167 offset:32
	ds_read_b128 v[180:183], v167 offset:4640
	ds_read_b128 v[184:187], v167 offset:64
	ds_read_b128 v[188:191], v167 offset:4672
	ds_read_b128 v[192:195], v167 offset:96
	ds_read_b128 v[196:199], v167 offset:4704
	v_mov_b32_e32 v200, 0
	v_mov_b32_e32 v201, 0
	v_mov_b32_e32 v202, 0
	v_mov_b32_e32 v83, 0
	v_exp_f32_e32 v34, v34
	v_exp_f32_e32 v35, v35
	v_add_f32_e32 v200, v200, v34
	v_exp_f32_e32 v36, v36
	v_add_f32_e32 v201, v201, v35
	v_exp_f32_e32 v37, v37
	s_waitcnt lgkmcnt(7)
	v_mfma_f32_32x32x16_f16 v[2:17], v[168:171], v[108:111], v[130:145]
	v_add_f32_e32 v202, v202, v36
	v_exp_f32_e32 v38, v38
	v_add_f32_e32 v83, v83, v37
	v_exp_f32_e32 v39, v39
	v_add_f32_e32 v200, v200, v38
	v_exp_f32_e32 v40, v40
	s_waitcnt lgkmcnt(6)
	v_mfma_f32_32x32x16_f16 v[18:33], v[172:175], v[108:111], v[130:145]
	v_add_f32_e32 v201, v201, v39
	v_exp_f32_e32 v41, v41
	v_add_f32_e32 v202, v202, v40
	v_exp_f32_e32 v42, v42
	v_add_f32_e32 v83, v83, v41
	v_exp_f32_e32 v43, v43
	s_waitcnt lgkmcnt(5)
	v_mfma_f32_32x32x16_f16 v[2:17], v[176:179], v[104:107], v[2:17]
	v_add_f32_e32 v200, v200, v42
	v_exp_f32_e32 v44, v44
	v_add_f32_e32 v201, v201, v43
	v_exp_f32_e32 v45, v45
	v_add_f32_e32 v202, v202, v44
	v_exp_f32_e32 v46, v46
	s_waitcnt lgkmcnt(4)
	v_mfma_f32_32x32x16_f16 v[18:33], v[180:183], v[104:107], v[18:33]
	v_add_f32_e32 v83, v83, v45
	v_exp_f32_e32 v47, v47
	v_add_f32_e32 v200, v200, v46
	v_exp_f32_e32 v48, v48
	v_add_f32_e32 v201, v201, v47
	v_exp_f32_e32 v49, v49
	s_waitcnt lgkmcnt(3)
	v_mfma_f32_32x32x16_f16 v[2:17], v[184:187], v[100:103], v[2:17]
	v_add_f32_e32 v202, v202, v48
	v_exp_f32_e32 v50, v50
	v_add_f32_e32 v83, v83, v49
	v_exp_f32_e32 v51, v51
	v_add_f32_e32 v200, v200, v50
	v_exp_f32_e32 v52, v52
	s_waitcnt lgkmcnt(2)
	v_mfma_f32_32x32x16_f16 v[18:33], v[188:191], v[100:103], v[18:33]
	v_add_f32_e32 v201, v201, v51
	v_exp_f32_e32 v53, v53
	v_add_f32_e32 v202, v202, v52
	v_exp_f32_e32 v54, v54
	v_add_f32_e32 v83, v83, v53
	v_exp_f32_e32 v55, v55
	s_waitcnt lgkmcnt(1)
	v_mfma_f32_32x32x16_f16 v[2:17], v[192:195], v[96:99], v[2:17]
	v_add_f32_e32 v200, v200, v54
	v_exp_f32_e32 v56, v56
	v_add_f32_e32 v201, v201, v55
	v_exp_f32_e32 v57, v57
	v_add_f32_e32 v202, v202, v56
	v_exp_f32_e32 v58, v58
	s_waitcnt lgkmcnt(0)
	v_mfma_f32_32x32x16_f16 v[18:33], v[196:199], v[96:99], v[18:33]
	ds_read_b128 v[204:207], v167 offset:9216
	ds_read_b128 v[208:211], v167 offset:13824
	ds_read_b128 v[212:215], v167 offset:9248
	ds_read_b128 v[216:219], v167 offset:13856
	ds_read_b128 v[220:223], v167 offset:9280
	ds_read_b128 v[224:227], v167 offset:13888
	ds_read_b128 v[228:231], v167 offset:9312
	ds_read_b128 v[232:235], v167 offset:13920
	v_add_f32_e32 v83, v83, v57
	v_exp_f32_e32 v59, v59
	v_add_f32_e32 v200, v200, v58
	v_exp_f32_e32 v60, v60
	v_add_f32_e32 v201, v201, v59
	v_exp_f32_e32 v61, v61
	v_add_f32_e32 v202, v202, v60
	v_exp_f32_e32 v62, v62
	v_add_f32_e32 v83, v83, v61
	v_exp_f32_e32 v63, v63
	v_add_f32_e32 v200, v200, v62
	v_exp_f32_e32 v64, v64
	v_add_f32_e32 v201, v201, v63
	v_exp_f32_e32 v65, v65
	v_add_f32_e32 v202, v202, v64
	v_add_f32_e32 v83, v83, v65
	v_add_f32_e32 v200, v200, v201
	v_add_f32_e32 v202, v202, v83
	v_add_f32_e32 v200, v200, v202
	v_add_f32_e32 v82, v82, v200
	v_max3_f32 v84, v2, v3, v4
	v_max3_f32 v85, v18, v19, v20
	v_max3_f32 v84, v84, v5, v6
	v_max3_f32 v85, v85, v21, v22
	v_max3_f32 v84, v84, v7, v8
	v_max3_f32 v85, v85, v23, v24
	v_max3_f32 v84, v84, v9, v10
	v_max3_f32 v85, v85, v25, v26
	v_max3_f32 v84, v84, v11, v12
	v_max3_f32 v85, v85, v27, v28
	v_max3_f32 v84, v84, v13, v14
	v_max3_f32 v85, v85, v29, v30
	v_max3_f32 v84, v84, v15, v16
	v_max3_f32 v85, v85, v31, v32
	v_max3_f32 v84, v84, v17, v33
	s_nop 0
	v_max_f32_e32 v84, v84, v85
	s_nop 0
	v_cmp_lt_f32_e32 vcc, s11, v84
	s_cbranch_vccnz .Lp1_rare_d0a
.Lp1_back_d0a:
	v_mov_b32_e32 v200, 0
	v_mov_b32_e32 v201, 0
	v_mov_b32_e32 v202, 0
	v_mov_b32_e32 v83, 0
	v_exp_f32_e32 v2, v2
	v_exp_f32_e32 v3, v3
	v_add_f32_e32 v200, v200, v2
	v_exp_f32_e32 v4, v4
	v_add_f32_e32 v201, v201, v3
	v_exp_f32_e32 v5, v5
	s_waitcnt lgkmcnt(7)
	v_mfma_f32_32x32x16_f16 v[34:49], v[204:207], v[108:111], v[130:145]
	v_add_f32_e32 v202, v202, v4
	v_exp_f32_e32 v6, v6
	v_add_f32_e32 v83, v83, v5
	v_exp_f32_e32 v7, v7
	v_add_f32_e32 v200, v200, v6
	v_exp_f32_e32 v8, v8
	s_waitcnt lgkmcnt(6)
	v_mfma_f32_32x32x16_f16 v[50:65], v[208:211], v[108:111], v[130:145]
	v_add_f32_e32 v201, v201, v7
	v_exp_f32_e32 v9, v9
	v_add_f32_e32 v202, v202, v8
	v_exp_f32_e32 v10, v10
	v_add_f32_e32 v83, v83, v9
	v_exp_f32_e32 v11, v11
	s_waitcnt lgkmcnt(5)
	v_mfma_f32_32x32x16_f16 v[34:49], v[212:215], v[104:107], v[34:49]
	v_add_f32_e32 v200, v200, v10
	v_exp_f32_e32 v12, v12
	v_add_f32_e32 v201, v201, v11
	v_exp_f32_e32 v13, v13
	v_add_f32_e32 v202, v202, v12
	v_exp_f32_e32 v14, v14
	s_waitcnt lgkmcnt(4)
	v_mfma_f32_32x32x16_f16 v[50:65], v[216:219], v[104:107], v[50:65]
	v_add_f32_e32 v83, v83, v13
	v_exp_f32_e32 v15, v15
	v_add_f32_e32 v200, v200, v14
	v_exp_f32_e32 v16, v16
	v_add_f32_e32 v201, v201, v15
	v_exp_f32_e32 v17, v17
	s_waitcnt lgkmcnt(3)
	v_mfma_f32_32x32x16_f16 v[34:49], v[220:223], v[100:103], v[34:49]
	v_add_f32_e32 v202, v202, v16
	v_exp_f32_e32 v18, v18
	v_add_f32_e32 v83, v83, v17
	v_exp_f32_e32 v19, v19
	v_add_f32_e32 v200, v200, v18
	v_exp_f32_e32 v20, v20
	s_waitcnt lgkmcnt(2)
	v_mfma_f32_32x32x16_f16 v[50:65], v[224:227], v[100:103], v[50:65]
	v_add_f32_e32 v201, v201, v19
	v_exp_f32_e32 v21, v21
	v_add_f32_e32 v202, v202, v20
	v_exp_f32_e32 v22, v22
	v_add_f32_e32 v83, v83, v21
	v_exp_f32_e32 v23, v23
	s_waitcnt lgkmcnt(1)
	v_mfma_f32_32x32x16_f16 v[34:49], v[228:231], v[96:99], v[34:49]
	v_add_f32_e32 v200, v200, v22
	v_exp_f32_e32 v24, v24
	v_add_f32_e32 v201, v201, v23
	v_exp_f32_e32 v25, v25
	v_add_f32_e32 v202, v202, v24
	v_exp_f32_e32 v26, v26
	s_waitcnt lgkmcnt(0)
	v_mfma_f32_32x32x16_f16 v[50:65], v[232:235], v[96:99], v[50:65]
	v_add_f32_e32 v83, v83, v25
	v_exp_f32_e32 v27, v27
	v_add_f32_e32 v200, v200, v26
	v_exp_f32_e32 v28, v28
	v_add_f32_e32 v201, v201, v27
	v_exp_f32_e32 v29, v29
	v_add_f32_e32 v202, v202, v28
	v_exp_f32_e32 v30, v30
	v_add_f32_e32 v83, v83, v29
	v_exp_f32_e32 v31, v31
	v_add_f32_e32 v200, v200, v30
	v_exp_f32_e32 v32, v32
	v_add_f32_e32 v201, v201, v31
	v_exp_f32_e32 v33, v33
	v_add_f32_e32 v202, v202, v32
	v_add_f32_e32 v83, v83, v33
	v_add_f32_e32 v200, v200, v201
	v_add_f32_e32 v202, v202, v83
	v_add_f32_e32 v200, v200, v202
	v_add_f32_e32 v82, v82, v200
	v_max3_f32 v84, v34, v35, v36
	v_max3_f32 v85, v50, v51, v52
	v_max3_f32 v84, v84, v37, v38
	v_max3_f32 v85, v85, v53, v54
	v_max3_f32 v84, v84, v39, v40
	v_max3_f32 v85, v85, v55, v56
	v_max3_f32 v84, v84, v41, v42
	v_max3_f32 v85, v85, v57, v58
	v_max3_f32 v84, v84, v43, v44
	v_max3_f32 v85, v85, v59, v60
	v_max3_f32 v84, v84, v45, v46
	v_max3_f32 v85, v85, v61, v62
	v_max3_f32 v84, v84, v47, v48
	v_max3_f32 v85, v85, v63, v64
	v_max3_f32 v84, v84, v49, v65
	s_nop 0
	v_max_f32_e32 v84, v84, v85
	s_nop 0
	v_cmp_lt_f32_e32 vcc, s11, v84
	s_cbranch_vccnz .Lp1_rare_d0b
.Lp1_back_d0b:
	s_waitcnt lgkmcnt(0)
	s_barrier
	s_waitcnt vmcnt(0)
	ds_write_b128 v77, v[112:115]
	ds_write_b128 v78, v[116:119]
	ds_write_b128 v77, v[120:123] offset:9216
	ds_write_b128 v78, v[124:127] offset:9216
	global_load_dwordx4 v[146:149], v128, s[24:25]
	global_load_dwordx4 v[150:153], v86, s[24:25]
	s_add_u32 s24, s24, 0x2000
	s_addc_u32 s25, s25, 0
	global_load_dwordx4 v[154:157], v128, s[24:25]
	global_load_dwordx4 v[158:161], v86, s[24:25]
	s_add_u32 s24, s24, 0x2000
	s_addc_u32 s25, s25, 0
	ds_read_b128 v[168:171], v87
	ds_read_b128 v[172:175], v87 offset:4608
	ds_read_b128 v[176:179], v87 offset:32
	ds_read_b128 v[180:183], v87 offset:4640
	ds_read_b128 v[184:187], v87 offset:64
	ds_read_b128 v[188:191], v87 offset:4672
	ds_read_b128 v[192:195], v87 offset:96
	ds_read_b128 v[196:199], v87 offset:4704
	v_mov_b32_e32 v200, 0
	v_mov_b32_e32 v201, 0
	v_mov_b32_e32 v202, 0
	v_mov_b32_e32 v83, 0
	v_exp_f32_e32 v34, v34
	v_exp_f32_e32 v35, v35
	v_add_f32_e32 v200, v200, v34
	v_exp_f32_e32 v36, v36
	v_add_f32_e32 v201, v201, v35
	v_exp_f32_e32 v37, v37
	s_waitcnt lgkmcnt(7)
	v_mfma_f32_32x32x16_f16 v[2:17], v[168:171], v[108:111], v[130:145]
	v_add_f32_e32 v202, v202, v36
	v_exp_f32_e32 v38, v38
	v_add_f32_e32 v83, v83, v37
	v_exp_f32_e32 v39, v39
	v_add_f32_e32 v200, v200, v38
	v_exp_f32_e32 v40, v40
	s_waitcnt lgkmcnt(6)
	v_mfma_f32_32x32x16_f16 v[18:33], v[172:175], v[108:111], v[130:145]
	v_add_f32_e32 v201, v201, v39
	v_exp_f32_e32 v41, v41
	v_add_f32_e32 v202, v202, v40
	v_exp_f32_e32 v42, v42
	v_add_f32_e32 v83, v83, v41
	v_exp_f32_e32 v43, v43
	s_waitcnt lgkmcnt(5)
	v_mfma_f32_32x32x16_f16 v[2:17], v[176:179], v[104:107], v[2:17]
	v_add_f32_e32 v200, v200, v42
	v_exp_f32_e32 v44, v44
	v_add_f32_e32 v201, v201, v43
	v_exp_f32_e32 v45, v45
	v_add_f32_e32 v202, v202, v44
	v_exp_f32_e32 v46, v46
	s_waitcnt lgkmcnt(4)
	v_mfma_f32_32x32x16_f16 v[18:33], v[180:183], v[104:107], v[18:33]
	v_add_f32_e32 v83, v83, v45
	v_exp_f32_e32 v47, v47
	v_add_f32_e32 v200, v200, v46
	v_exp_f32_e32 v48, v48
	v_add_f32_e32 v201, v201, v47
	v_exp_f32_e32 v49, v49
	s_waitcnt lgkmcnt(3)
	v_mfma_f32_32x32x16_f16 v[2:17], v[184:187], v[100:103], v[2:17]
	v_add_f32_e32 v202, v202, v48
	v_exp_f32_e32 v50, v50
	v_add_f32_e32 v83, v83, v49
	v_exp_f32_e32 v51, v51
	v_add_f32_e32 v200, v200, v50
	v_exp_f32_e32 v52, v52
	s_waitcnt lgkmcnt(2)
	v_mfma_f32_32x32x16_f16 v[18:33], v[188:191], v[100:103], v[18:33]
	v_add_f32_e32 v201, v201, v51
	v_exp_f32_e32 v53, v53
	v_add_f32_e32 v202, v202, v52
	v_exp_f32_e32 v54, v54
	v_add_f32_e32 v83, v83, v53
	v_exp_f32_e32 v55, v55
	s_waitcnt lgkmcnt(1)
	v_mfma_f32_32x32x16_f16 v[2:17], v[192:195], v[96:99], v[2:17]
	v_add_f32_e32 v200, v200, v54
	v_exp_f32_e32 v56, v56
	v_add_f32_e32 v201, v201, v55
	v_exp_f32_e32 v57, v57
	v_add_f32_e32 v202, v202, v56
	v_exp_f32_e32 v58, v58
	s_waitcnt lgkmcnt(0)
	v_mfma_f32_32x32x16_f16 v[18:33], v[196:199], v[96:99], v[18:33]
	ds_read_b128 v[204:207], v87 offset:9216
	ds_read_b128 v[208:211], v87 offset:13824
	ds_read_b128 v[212:215], v87 offset:9248
	ds_read_b128 v[216:219], v87 offset:13856
	ds_read_b128 v[220:223], v87 offset:9280
	ds_read_b128 v[224:227], v87 offset:13888
	ds_read_b128 v[228:231], v87 offset:9312
	ds_read_b128 v[232:235], v87 offset:13920
	v_add_f32_e32 v83, v83, v57
	v_exp_f32_e32 v59, v59
	v_add_f32_e32 v200, v200, v58
	v_exp_f32_e32 v60, v60
	v_add_f32_e32 v201, v201, v59
	v_exp_f32_e32 v61, v61
	v_add_f32_e32 v202, v202, v60
	v_exp_f32_e32 v62, v62
	v_add_f32_e32 v83, v83, v61
	v_exp_f32_e32 v63, v63
	v_add_f32_e32 v200, v200, v62
	v_exp_f32_e32 v64, v64
	v_add_f32_e32 v201, v201, v63
	v_exp_f32_e32 v65, v65
	v_add_f32_e32 v202, v202, v64
	v_add_f32_e32 v83, v83, v65
	v_add_f32_e32 v200, v200, v201
	v_add_f32_e32 v202, v202, v83
	v_add_f32_e32 v200, v200, v202
	v_add_f32_e32 v82, v82, v200
	v_max3_f32 v84, v2, v3, v4
	v_max3_f32 v85, v18, v19, v20
	v_max3_f32 v84, v84, v5, v6
	v_max3_f32 v85, v85, v21, v22
	v_max3_f32 v84, v84, v7, v8
	v_max3_f32 v85, v85, v23, v24
	v_max3_f32 v84, v84, v9, v10
	v_max3_f32 v85, v85, v25, v26
	v_max3_f32 v84, v84, v11, v12
	v_max3_f32 v85, v85, v27, v28
	v_max3_f32 v84, v84, v13, v14
	v_max3_f32 v85, v85, v29, v30
	v_max3_f32 v84, v84, v15, v16
	v_max3_f32 v85, v85, v31, v32
	v_max3_f32 v84, v84, v17, v33
	s_nop 0
	v_max_f32_e32 v84, v84, v85
	s_nop 0
	v_cmp_lt_f32_e32 vcc, s11, v84
	s_cbranch_vccnz .Lp1_rare_d1a

.Lp1_back_d1b:
	s_add_i32 s15, s15, 4
	s_cmp_lt_u32 s15, 32
	s_waitcnt lgkmcnt(0)
	s_barrier
	s_cbranch_scc1 .Lp1_loop
	s_branch .Lp1_fin

.Lp1_rare_d0b:
	s_nop 1
	v_cndmask_b32_e32 v84, 0, v84, vcc
	v_exp_f32_e64 v85, -v84
	v_add_f32_e32 v81, v81, v84
	v_sub_f32_e32 v34, v34, v84
	v_sub_f32_e32 v35, v35, v84
	v_sub_f32_e32 v36, v36, v84
	v_sub_f32_e32 v37, v37, v84
	v_sub_f32_e32 v38, v38, v84
	v_sub_f32_e32 v39, v39, v84
	v_sub_f32_e32 v40, v40, v84
	v_sub_f32_e32 v41, v41, v84
	v_sub_f32_e32 v42, v42, v84
	v_sub_f32_e32 v43, v43, v84
	v_sub_f32_e32 v44, v44, v84
	v_sub_f32_e32 v45, v45, v84
	v_sub_f32_e32 v46, v46, v84
	v_sub_f32_e32 v47, v47, v84
	v_sub_f32_e32 v48, v48, v84
	v_sub_f32_e32 v49, v49, v84
	v_sub_f32_e32 v50, v50, v84
	v_sub_f32_e32 v51, v51, v84
	v_sub_f32_e32 v52, v52, v84
	v_sub_f32_e32 v53, v53, v84
	v_sub_f32_e32 v54, v54, v84
	v_sub_f32_e32 v55, v55, v84
	v_sub_f32_e32 v56, v56, v84
	v_sub_f32_e32 v57, v57, v84
	v_sub_f32_e32 v58, v58, v84
	v_sub_f32_e32 v59, v59, v84
	v_sub_f32_e32 v60, v60, v84
	v_sub_f32_e32 v61, v61, v84
	v_sub_f32_e32 v62, v62, v84
	v_sub_f32_e32 v63, v63, v84
	v_sub_f32_e32 v64, v64, v84
	v_sub_f32_e32 v65, v65, v84
	v_mul_f32_e32 v82, v82, v85
	v_xor_b32_e32 v130, 0x80000000, v81
	s_mov_b32 s11, 0x41000000
	v_mov_b32_e32 v131, v130
	v_mov_b32_e32 v132, v130
	v_mov_b32_e32 v133, v130
	v_mov_b32_e32 v134, v130
	v_mov_b32_e32 v135, v130
	v_mov_b32_e32 v136, v130
	v_mov_b32_e32 v137, v130
	v_mov_b32_e32 v138, v130
	v_mov_b32_e32 v139, v130
	v_mov_b32_e32 v140, v130
	v_mov_b32_e32 v141, v130
	v_mov_b32_e32 v142, v130
	v_mov_b32_e32 v143, v130
	v_mov_b32_e32 v144, v130
	v_mov_b32_e32 v145, v130
	s_branch .Lp1_back_d0b
.Lp1_rare_d1a:
	s_nop 1
	v_cndmask_b32_e32 v84, 0, v84, vcc
	v_exp_f32_e64 v85, -v84
	v_add_f32_e32 v81, v81, v84
	v_sub_f32_e32 v2, v2, v84
	v_sub_f32_e32 v3, v3, v84
	v_sub_f32_e32 v4, v4, v84
	v_sub_f32_e32 v5, v5, v84
	v_sub_f32_e32 v6, v6, v84
	v_sub_f32_e32 v7, v7, v84
	v_sub_f32_e32 v8, v8, v84
	v_sub_f32_e32 v9, v9, v84
	v_sub_f32_e32 v10, v10, v84
	v_sub_f32_e32 v11, v11, v84
	v_sub_f32_e32 v12, v12, v84
	v_sub_f32_e32 v13, v13, v84
	v_sub_f32_e32 v14, v14, v84
	v_sub_f32_e32 v15, v15, v84
	v_sub_f32_e32 v16, v16, v84
	v_sub_f32_e32 v17, v17, v84
	v_sub_f32_e32 v18, v18, v84
	v_sub_f32_e32 v19, v19, v84
	v_sub_f32_e32 v20, v20, v84
	v_sub_f32_e32 v21, v21, v84
	v_sub_f32_e32 v22, v22, v84
	v_sub_f32_e32 v23, v23, v84
	v_sub_f32_e32 v24, v24, v84
	v_sub_f32_e32 v25, v25, v84
	v_sub_f32_e32 v26, v26, v84
	v_sub_f32_e32 v27, v27, v84
	v_sub_f32_e32 v28, v28, v84
	v_sub_f32_e32 v29, v29, v84
	v_sub_f32_e32 v30, v30, v84
	v_sub_f32_e32 v31, v31, v84
	v_sub_f32_e32 v32, v32, v84
	v_sub_f32_e32 v33, v33, v84
	v_mul_f32_e32 v82, v82, v85
	v_xor_b32_e32 v130, 0x80000000, v81
	s_mov_b32 s11, 0x41000000
	v_mov_b32_e32 v131, v130
	v_mov_b32_e32 v132, v130
	v_mov_b32_e32 v133, v130
	v_mov_b32_e32 v134, v130
	v_mov_b32_e32 v135, v130
	v_mov_b32_e32 v136, v130
	v_mov_b32_e32 v137, v130
	v_mov_b32_e32 v138, v130
	v_mov_b32_e32 v139, v130
	v_mov_b32_e32 v140, v130
	v_mov_b32_e32 v141, v130
	v_mov_b32_e32 v142, v130
	v_mov_b32_e32 v143, v130
	v_mov_b32_e32 v144, v130
	v_mov_b32_e32 v145, v130
	s_branch .Lp1_back_d1a

.Lp1_fin:
	s_lshl_b64 s[0:1], s[20:21], 1
	s_add_u32 s0, s18, s0
	s_addc_u32 s1, s19, s1
	global_load_dwordx4 v[2:5], v[66:67], off
	global_load_dwordx4 v[6:9], v[68:69], off
	v_lshlrev_b32_e32 v10, 1, v79
	global_load_dwordx4 v[10:13], v10, s[0:1]
	v_lshlrev_b32_e32 v14, 1, v80
	global_load_dwordx4 v[14:17], v14, s[0:1]
	v_mov_b32_e32 v200, 0
	v_mov_b32_e32 v201, 0
	v_mov_b32_e32 v202, 0
	v_mov_b32_e32 v83, 0
	v_exp_f32_e32 v34, v34
	v_exp_f32_e32 v35, v35
	v_add_f32_e32 v200, v200, v34
	v_exp_f32_e32 v36, v36
	v_add_f32_e32 v201, v201, v35
	v_exp_f32_e32 v37, v37
	v_add_f32_e32 v202, v202, v36
	v_exp_f32_e32 v38, v38
	v_add_f32_e32 v83, v83, v37
	v_exp_f32_e32 v39, v39
	v_add_f32_e32 v200, v200, v38
	v_exp_f32_e32 v40, v40
	v_add_f32_e32 v201, v201, v39
	v_exp_f32_e32 v41, v41
	v_add_f32_e32 v202, v202, v40
	v_exp_f32_e32 v42, v42
	v_add_f32_e32 v83, v83, v41
	v_exp_f32_e32 v43, v43
	v_add_f32_e32 v200, v200, v42
	v_exp_f32_e32 v44, v44
	v_add_f32_e32 v201, v201, v43
	v_exp_f32_e32 v45, v45
	v_add_f32_e32 v202, v202, v44
	v_exp_f32_e32 v46, v46
	v_add_f32_e32 v83, v83, v45
	v_exp_f32_e32 v47, v47
	v_add_f32_e32 v200, v200, v46
	v_exp_f32_e32 v48, v48
	v_add_f32_e32 v201, v201, v47
	v_exp_f32_e32 v49, v49
	v_add_f32_e32 v202, v202, v48
	v_exp_f32_e32 v50, v50
	v_add_f32_e32 v83, v83, v49
	v_exp_f32_e32 v51, v51
	v_add_f32_e32 v200, v200, v50
	v_exp_f32_e32 v52, v52
	v_add_f32_e32 v201, v201, v51
	v_exp_f32_e32 v53, v53
	v_add_f32_e32 v202, v202, v52
	v_exp_f32_e32 v54, v54
	v_add_f32_e32 v83, v83, v53
	v_exp_f32_e32 v55, v55
	v_add_f32_e32 v200, v200, v54
	v_exp_f32_e32 v56, v56
	v_add_f32_e32 v201, v201, v55
	v_exp_f32_e32 v57, v57
	v_add_f32_e32 v202, v202, v56
	v_exp_f32_e32 v58, v58
	v_add_f32_e32 v83, v83, v57
	v_exp_f32_e32 v59, v59
	v_add_f32_e32 v200, v200, v58
	v_exp_f32_e32 v60, v60
	v_add_f32_e32 v201, v201, v59
	v_exp_f32_e32 v61, v61
	v_add_f32_e32 v202, v202, v60
	v_exp_f32_e32 v62, v62
	v_add_f32_e32 v83, v83, v61
	v_exp_f32_e32 v63, v63
	v_add_f32_e32 v200, v200, v62
	v_exp_f32_e32 v64, v64
	v_add_f32_e32 v201, v201, v63
	v_exp_f32_e32 v65, v65
	v_add_f32_e32 v202, v202, v64
	v_add_f32_e32 v83, v83, v65
	v_add_f32_e32 v200, v200, v201
	v_add_f32_e32 v202, v202, v83
	v_add_f32_e32 v200, v200, v202
	v_add_f32_e32 v82, v82, v200
	s_barrier
	v_mbcnt_lo_u32_b32 v21, -1, 0
	v_mbcnt_hi_u32_b32 v21, -1, v21
	v_and_b32_e32 v23, 64, v21
	v_xor_b32_e32 v22, 32, v21
	v_add_u32_e32 v24, 64, v23
	v_cmp_lt_i32_e32 vcc, v22, v24
	v_cndmask_b32_e32 v21, v21, v22, vcc
	v_lshlrev_b32_e32 v21, 2, v21
	ds_bpermute_b32 v22, v21, v81
	v_mov_b32_e32 v18, v82
	ds_bpermute_b32 v19, v21, v18
	v_max_f32_e32 v21, v81, v81
	s_mov_b32 s15, 0
	s_waitcnt lgkmcnt(1)
	v_max_f32_e32 v20, v22, v22
	v_max_f32_e32 v20, v21, v20
	v_sub_f32_e32 v22, v22, v20
	v_sub_f32_e32 v21, v81, v20
	v_exp_f32_e32 v22, v22
	v_exp_f32_e32 v21, v21
	s_lshl_b64 s[18:19], s[14:15], 18
	v_mov_b32_e32 v131, 0
	s_waitcnt lgkmcnt(0)
	v_mul_f32_e32 v19, v22, v19
	v_fmac_f32_e32 v19, v18, v21
	v_div_scale_f32 v18, s[10:11], v19, v19, 1.0
	s_movk_i32 s10, 0x60
	s_nop 0
	v_mad_u32_u24 v188, v73, s10, v74
	v_mad_u32_u24 v189, v75, s10, v74
	s_waitcnt vmcnt(3)
	ds_write_b128 v77, v[2:5]
	s_waitcnt vmcnt(2)
	ds_write_b128 v78, v[6:9]
	v_lshlrev_b32_e32 v2, 1, v188
	s_waitcnt vmcnt(1)
	ds_write_b128 v2, v[10:13]
	v_lshlrev_b32_e32 v2, 1, v189
	s_mul_i32 s10, s14, 0x1200
	s_waitcnt vmcnt(0)
	ds_write_b128 v2, v[14:17]
	s_add_i32 s10, s10, 0xa800
	v_lshrrev_b32_e32 v2, 2, v0
	v_and_or_b32 v3, v2, 3, v1
	s_movk_i32 s11, 0x48
	v_mov_b32_e32 v5, s10
	v_add_u32_e32 v4, s10, v76
	v_mad_u32_u24 v5, v3, s11, v5
	s_lshl_b64 s[10:11], s[12:13], 24
	s_and_b32 s13, s2, 15
	s_lshl_b32 s13, s13, 20
	v_and_b32_e32 v0, 3, v0
	s_or_b32 s10, s10, s13
	v_and_or_b32 v0, v2, 4, v0
	s_add_u32 s10, s10, s18
	v_lshlrev_b32_e32 v0, 3, v0
	v_mul_u32_u24_e32 v2, 0xc0, v3
	v_lshlrev_b32_e32 v3, 13, v72
	s_addc_u32 s11, s11, s19
	v_or_b32_e32 v185, v2, v0
	v_or_b32_e32 v2, v3, v164
	s_add_u32 s10, s4, s10
	v_lshlrev_b32_e32 v130, 2, v2
	s_addc_u32 s11, s5, s11
	v_lshl_add_u64 v[2:3], s[10:11], 0, v[130:131]
	s_mov_b64 s[18:19], 0x80
	v_lshl_add_u64 v[132:133], v[2:3], 0, s[18:19]
	v_or_b32_e32 v2, 0x36000, v130
	v_mov_b32_e32 v3, v131
	v_lshl_add_u64 v[134:135], s[10:11], 0, v[2:3]
	v_or_b32_e32 v2, 0x2000, v130
	v_lshl_add_u64 v[2:3], s[10:11], 0, v[2:3]
	v_lshl_add_u64 v[136:137], v[2:3], 0, s[18:19]
	v_or_b32_e32 v2, 0x34000, v130
	v_mov_b32_e32 v3, v131
	v_rcp_f32_e32 v21, v18
	v_lshl_add_u64 v[138:139], s[10:11], 0, v[2:3]
	v_or_b32_e32 v2, 0x4000, v130
	v_lshl_add_u64 v[2:3], s[10:11], 0, v[2:3]
	v_lshl_add_u64 v[140:141], v[2:3], 0, s[18:19]
	v_or_b32_e32 v2, 0x32000, v130
	v_mov_b32_e32 v3, v131
	v_lshl_add_u64 v[142:143], s[10:11], 0, v[2:3]
	v_or_b32_e32 v2, 0x6000, v130
	v_fma_f32 v22, -v18, v21, 1.0
	v_lshl_add_u64 v[2:3], s[10:11], 0, v[2:3]
	v_fmac_f32_e32 v21, v22, v21
	v_div_scale_f32 v22, vcc, 1.0, v19, 1.0
	v_lshl_add_u64 v[144:145], v[2:3], 0, s[18:19]
	v_or_b32_e32 v2, 0x30000, v130
	v_mov_b32_e32 v3, v131
	v_mul_f32_e32 v24, v22, v21
	v_lshl_add_u64 v[146:147], s[10:11], 0, v[2:3]
	v_or_b32_e32 v2, 0x10000, v130
	v_fma_f32 v25, -v18, v24, v22
	v_lshl_add_u64 v[2:3], s[10:11], 0, v[2:3]
	v_fmac_f32_e32 v24, v25, v21
	v_lshl_add_u64 v[148:149], v[2:3], 0, s[18:19]
	v_or_b32_e32 v2, 0x26000, v130
	v_mov_b32_e32 v3, v131
	v_fma_f32 v18, -v18, v24, v22
	v_lshl_add_u64 v[150:151], s[10:11], 0, v[2:3]
	v_or_b32_e32 v2, 0x12000, v130
	v_div_fmas_f32 v18, v18, v21, v24
	v_lshlrev_b32_e32 v184, 2, v72
	v_lshl_add_u64 v[2:3], s[10:11], 0, v[2:3]
	v_div_fixup_f32 v18, v18, v19, 1.0
	v_or_b32_e32 v19, v184, v23
	v_lshl_add_u64 v[152:153], v[2:3], 0, s[18:19]
	v_or_b32_e32 v2, 0x24000, v130
	v_mov_b32_e32 v3, v131
	v_lshlrev_b32_e32 v19, 2, v19
	v_lshl_add_u64 v[154:155], s[10:11], 0, v[2:3]
	v_or_b32_e32 v2, 0x14000, v130
	ds_bpermute_b32 v33, v19, v20 offset:36
	ds_bpermute_b32 v32, v19, v20 offset:40
	ds_bpermute_b32 v35, v19, v20 offset:44
	ds_bpermute_b32 v34, v19, v20 offset:64
	ds_bpermute_b32 v37, v19, v20 offset:68
	ds_bpermute_b32 v36, v19, v20 offset:72
	ds_bpermute_b32 v39, v19, v20 offset:76
	ds_bpermute_b32 v38, v19, v20 offset:96
	ds_bpermute_b32 v41, v19, v20 offset:100
	ds_bpermute_b32 v40, v19, v20 offset:104
	ds_bpermute_b32 v43, v19, v20 offset:108
	v_lshl_add_u64 v[2:3], s[10:11], 0, v[2:3]
	ds_bpermute_b32 v46, v19, v20 offset:32
	ds_bpermute_b32 v47, v19, v20 offset:12
	ds_bpermute_b32 v42, v19, v20 offset:8
	ds_bpermute_b32 v45, v19, v20 offset:4
	ds_bpermute_b32 v44, v19, v20
	ds_bpermute_b32 v183, v19, v18
	ds_bpermute_b32 v182, v19, v18 offset:4
	ds_bpermute_b32 v181, v19, v18 offset:8
	ds_bpermute_b32 v180, v19, v18 offset:12
	ds_bpermute_b32 v179, v19, v18 offset:32
	ds_bpermute_b32 v178, v19, v18 offset:36
	ds_bpermute_b32 v177, v19, v18 offset:40
	ds_bpermute_b32 v176, v19, v18 offset:44
	ds_bpermute_b32 v175, v19, v18 offset:64
	ds_bpermute_b32 v174, v19, v18 offset:68
	ds_bpermute_b32 v173, v19, v18 offset:72
	ds_bpermute_b32 v172, v19, v18 offset:76
	ds_bpermute_b32 v171, v19, v18 offset:96
	ds_bpermute_b32 v170, v19, v18 offset:100
	ds_bpermute_b32 v169, v19, v18 offset:104
	ds_bpermute_b32 v168, v19, v18 offset:108
	v_lshl_add_u64 v[156:157], v[2:3], 0, s[18:19]
	v_or_b32_e32 v2, 0x22000, v130
	v_mov_b32_e32 v3, v131
	v_lshl_add_u64 v[158:159], s[10:11], 0, v[2:3]
	v_or_b32_e32 v2, 0x16000, v130
	v_lshl_add_u64 v[2:3], s[10:11], 0, v[2:3]
	v_lshl_add_u64 v[160:161], v[2:3], 0, s[18:19]
	v_or_b32_e32 v2, 0x20000, v130
	v_mov_b32_e32 v3, v131
	v_add_u32_e32 v187, v4, v1
	v_lshl_add_u64 v[162:163], s[10:11], 0, v[2:3]
	s_mov_b64 s[10:11], 0
	s_movk_i32 s13, 0x3000
	s_waitcnt lgkmcnt(14)
	v_xor_b32_e32 v63, 0x80000000, v43
	v_xor_b32_e32 v62, 0x80000000, v40
	v_xor_b32_e32 v61, 0x80000000, v41
	v_xor_b32_e32 v60, 0x80000000, v38
	v_xor_b32_e32 v59, 0x80000000, v39
	v_xor_b32_e32 v58, 0x80000000, v36
	v_xor_b32_e32 v57, 0x80000000, v37
	v_xor_b32_e32 v56, 0x80000000, v34
	v_xor_b32_e32 v55, 0x80000000, v35
	v_xor_b32_e32 v54, 0x80000000, v32
	v_xor_b32_e32 v53, 0x80000000, v33
	v_add_u32_e32 v186, v5, v0
	v_xor_b32_e32 v52, 0x80000000, v46
	v_xor_b32_e32 v51, 0x80000000, v47
	v_xor_b32_e32 v50, 0x80000000, v42
	v_xor_b32_e32 v49, 0x80000000, v45
	v_xor_b32_e32 v48, 0x80000000, v44
	v_mov_b32_e32 v0, v131
	v_mov_b32_e32 v1, v131
	v_mov_b32_e32 v2, v131
	v_mov_b32_e32 v4, v131
	v_mov_b32_e32 v5, v131
	v_mov_b32_e32 v6, v131
	v_mov_b32_e32 v7, v131
	v_mov_b32_e32 v8, v131
	v_mov_b32_e32 v9, v131
	v_mov_b32_e32 v10, v131
	v_mov_b32_e32 v11, v131
	v_mov_b32_e32 v12, v131
	v_mov_b32_e32 v13, v131
	v_mov_b32_e32 v14, v131
	v_mov_b32_e32 v15, v131
	v_mov_b32_e32 v16, v131
	v_mov_b32_e32 v17, v131
	v_mov_b32_e32 v18, v131
	v_mov_b32_e32 v19, v131
	v_mov_b32_e32 v20, v131
	v_mov_b32_e32 v21, v131
	v_mov_b32_e32 v22, v131
	v_mov_b32_e32 v23, v131
	v_mov_b32_e32 v24, v131
	v_mov_b32_e32 v25, v131
	v_mov_b32_e32 v26, v131
	v_mov_b32_e32 v27, v131
	v_mov_b32_e32 v28, v131
	v_mov_b32_e32 v29, v131
	v_mov_b32_e32 v30, v131
	v_mov_b32_e32 v31, v131
	v_add_u32_e32 v131, 0x800, v187
	s_waitcnt lgkmcnt(0)
	s_barrier

	.amdhsa_kernel _Z11attn_kernelILi0EEvPKDF16_S1_S1_PKfS3_PfPDF16_
		.amdhsa_group_segment_fixed_size 61440
		.amdhsa_private_segment_fixed_size 0
		.amdhsa_kernarg_size 56
		.amdhsa_user_sgpr_count 2
		.amdhsa_user_sgpr_dispatch_ptr 0
		.amdhsa_user_sgpr_queue_ptr 0
		.amdhsa_user_sgpr_kernarg_segment_ptr 1
		.amdhsa_user_sgpr_dispatch_id 0
		.amdhsa_user_sgpr_kernarg_preload_length 0
		.amdhsa_user_sgpr_kernarg_preload_offset 0
		.amdhsa_user_sgpr_private_segment_size 0
		.amdhsa_uses_dynamic_stack 0
		.amdhsa_enable_private_segment 0
		.amdhsa_system_sgpr_workgroup_id_x 1
		.amdhsa_system_sgpr_workgroup_id_y 0
		.amdhsa_system_sgpr_workgroup_id_z 0
		.amdhsa_system_sgpr_workgroup_info 0
		.amdhsa_system_vgpr_workitem_id 0
		.amdhsa_next_free_vgpr 236
		.amdhsa_next_free_sgpr 96
		.amdhsa_accum_offset 236
		.amdhsa_reserve_vcc 1
		.amdhsa_float_round_mode_32 0
		.amdhsa_float_round_mode_16_64 0
		.amdhsa_float_denorm_mode_32 3
		.amdhsa_float_denorm_mode_16_64 3
		.amdhsa_dx10_clamp 1
		.amdhsa_ieee_mode 1
		.amdhsa_fp16_overflow 0
		.amdhsa_tg_split 0
		.amdhsa_exception_fp_ieee_invalid_op 0
		.amdhsa_exception_fp_denorm_src 0
		.amdhsa_exception_fp_ieee_div_zero 0
		.amdhsa_exception_fp_ieee_overflow 0
		.amdhsa_exception_fp_ieee_underflow 0
		.amdhsa_exception_fp_ieee_inexact 0
		.amdhsa_exception_int_div_zero 0
	.end_amdhsa_kernel

amdhsa.kernels:
  - .agpr_count:     0
    .args:
      - .actual_access:  read_only
        .address_space:  global
        .offset:         0
        .size:           8
        .value_kind:     global_buffer
      - .actual_access:  read_only
        .address_space:  global
        .offset:         8
        .size:           8
        .value_kind:     global_buffer
      - .actual_access:  read_only
        .address_space:  global
        .offset:         16
        .size:           8
        .value_kind:     global_buffer
      - .actual_access:  read_only
        .address_space:  global
        .offset:         24
        .size:           8
        .value_kind:     global_buffer
      - .actual_access:  read_only
        .address_space:  global
        .offset:         32
        .size:           8
        .value_kind:     global_buffer
      - .actual_access:  write_only
        .address_space:  global
        .offset:         40
        .size:           8
        .value_kind:     global_buffer
      - .actual_access:  write_only
        .address_space:  global
        .offset:         48
        .size:           8
        .value_kind:     global_buffer
    .group_segment_fixed_size: 0
    .kernarg_segment_align: 8
    .kernarg_segment_size: 56
    .language:       OpenCL C
    .language_version:
      - 2
      - 0
    .max_flat_workgroup_size: 256
    .name:           _Z10cvt_kernelPKfS0_S0_S0_S0_PDF16_S1_
    .private_segment_fixed_size: 0
    .sgpr_count:     22
    .sgpr_spill_count: 0
    .symbol:         _Z10cvt_kernelPKfS0_S0_S0_S0_PDF16_S1_.kd
    .uniform_work_group_size: 1
    .uses_dynamic_stack: false
    .vgpr_count:     14
    .vgpr_spill_count: 0
    .wavefront_size: 64
  - .agpr_count:     0
    .args:
      - .actual_access:  read_only
        .address_space:  global
        .offset:         0
        .size:           8
        .value_kind:     global_buffer
      - .actual_access:  read_only
        .address_space:  global
        .offset:         8
        .size:           8
        .value_kind:     global_buffer
      - .actual_access:  write_only
        .address_space:  global
        .offset:         16
        .size:           8
        .value_kind:     global_buffer
      - .actual_access:  write_only
        .address_space:  global
        .offset:         24
        .size:           8
        .value_kind:     global_buffer
    .group_segment_fixed_size: 18432
    .kernarg_segment_align: 8
    .kernarg_segment_size: 32
    .language:       OpenCL C
    .language_version:
      - 2
      - 0
    .max_flat_workgroup_size: 256
    .name:           _Z12stats_kernelPKDF16_S0_PfS1_
    .private_segment_fixed_size: 0
    .sgpr_count:     19
    .sgpr_spill_count: 0
    .symbol:         _Z12stats_kernelPKDF16_S0_PfS1_.kd
    .uniform_work_group_size: 1
    .uses_dynamic_stack: false
    .vgpr_count:     100
    .vgpr_spill_count: 0
    .wavefront_size: 64
  - .agpr_count:     0
    .args:
      - .actual_access:  read_only
        .address_space:  global
        .offset:         0
        .size:           8
        .value_kind:     global_buffer
      - .actual_access:  read_only
        .address_space:  global
        .offset:         8
        .size:           8
        .value_kind:     global_buffer
      - .actual_access:  read_only
        .address_space:  global
        .offset:         16
        .size:           8
        .value_kind:     global_buffer
      - .actual_access:  read_only
        .address_space:  global
        .offset:         24
        .size:           8
        .value_kind:     global_buffer
      - .actual_access:  write_only
        .address_space:  global
        .offset:         32
        .size:           8
        .value_kind:     global_buffer
      - .actual_access:  write_only
        .address_space:  global
        .offset:         40
        .size:           8
        .value_kind:     global_buffer
      - .actual_access:  write_only
        .address_space:  global
        .offset:         48
        .size:           8
        .value_kind:     global_buffer
      - .actual_access:  read_only
        .address_space:  global
        .offset:         56
        .size:           8
        .value_kind:     global_buffer
      - .offset:         64
        .size:           4
        .value_kind:     by_value
    .group_segment_fixed_size: 0
    .kernarg_segment_align: 8
    .kernarg_segment_size: 68
    .language:       OpenCL C
    .language_version:
      - 2
      - 0
    .max_flat_workgroup_size: 512
    .name:           _Z11gemm_kernelILi256ELi192ELi4ELi2ELi0EEvPKDF16_S1_PKfS3_PDF16_S4_S4_Pfi
    .private_segment_fixed_size: 0
    .sgpr_count:     27
    .sgpr_spill_count: 0
    .symbol:         _Z11gemm_kernelILi256ELi192ELi4ELi2ELi0EEvPKDF16_S1_PKfS3_PDF16_S4_S4_Pfi.kd
    .uniform_work_group_size: 1
    .uses_dynamic_stack: false
    .vgpr_count:     249
    .vgpr_spill_count: 0
    .wavefront_size: 64
  - .agpr_count:     0
    .args:
      - .actual_access:  read_only
        .address_space:  global
        .offset:         0
        .size:           8
        .value_kind:     global_buffer
      - .actual_access:  read_only
        .address_space:  global
        .offset:         8
        .size:           8
        .value_kind:     global_buffer
      - .actual_access:  read_only
        .address_space:  global
        .offset:         16
        .size:           8
        .value_kind:     global_buffer
      - .actual_access:  read_only
        .address_space:  global
        .offset:         24
        .size:           8
        .value_kind:     global_buffer
      - .actual_access:  read_only
        .address_space:  global
        .offset:         32
        .size:           8
        .value_kind:     global_buffer
      - .actual_access:  read_only
        .address_space:  global
        .offset:         40
        .size:           8
        .value_kind:     global_buffer
      - .actual_access:  read_only
        .address_space:  global
        .offset:         48
        .size:           8
        .value_kind:     global_buffer
      - .actual_access:  write_only
        .address_space:  global
        .offset:         56
        .size:           8
        .value_kind:     global_buffer
      - .offset:         64
        .size:           4
        .value_kind:     by_value
    .group_segment_fixed_size: 0
    .kernarg_segment_align: 8
    .kernarg_segment_size: 68
    .language:       OpenCL C
    .language_version:
      - 2
      - 0
    .max_flat_workgroup_size: 512
    .name:           _Z11gemm_kernelILi128ELi128ELi4ELi2ELi1EEvPKDF16_S1_PKfS3_PDF16_S4_S4_Pfi
    .private_segment_fixed_size: 0
    .sgpr_count:     19
    .sgpr_spill_count: 0
    .symbol:         _Z11gemm_kernelILi128ELi128ELi4ELi2ELi1EEvPKDF16_S1_PKfS3_PDF16_S4_S4_Pfi.kd
    .uniform_work_group_size: 1
    .uses_dynamic_stack: false
    .vgpr_count:     88
    .vgpr_spill_count: 0
    .wavefront_size: 64
  - .agpr_count:     0
    .args:
      - .actual_access:  read_only
        .address_space:  global
        .offset:         0
        .size:           8
        .value_kind:     global_buffer
      - .actual_access:  read_only
        .address_space:  global
        .offset:         8
        .size:           8
        .value_kind:     global_buffer
      - .actual_access:  read_only
        .address_space:  global
        .offset:         16
        .size:           8
        .value_kind:     global_buffer
      - .actual_access:  read_only
        .address_space:  global
        .offset:         24
        .size:           8
        .value_kind:     global_buffer
      - .actual_access:  read_only
        .address_space:  global
        .offset:         32
        .size:           8
        .value_kind:     global_buffer
      - .actual_access:  write_only
        .address_space:  global
        .offset:         40
        .size:           8
        .value_kind:     global_buffer
      - .actual_access:  write_only
        .address_space:  global
        .offset:         48
        .size:           8
        .value_kind:     global_buffer
    .group_segment_fixed_size: 61440
    .kernarg_segment_align: 8
    .kernarg_segment_size: 56
    .language:       OpenCL C
    .language_version:
      - 2
      - 0
    .max_flat_workgroup_size: 256
    .name:           _Z11attn_kernelILi0EEvPKDF16_S1_S1_PKfS3_PfPDF16_
    .private_segment_fixed_size: 0
    .sgpr_count:     30
    .sgpr_spill_count: 0
    .symbol:         _Z11attn_kernelILi0EEvPKDF16_S1_S1_PKfS3_PfPDF16_.kd
    .uniform_work_group_size: 1
    .uses_dynamic_stack: false
    .vgpr_count:     236
    .vgpr_spill_count: 0
    .wavefront_size: 64
